# nt hint also on the SSD scan's chunk loads (P3)
# baseline (speedup 1.0000x reference)
.LBB0_362:
	s_and_b64 s[28:29], s[66:67], exec
	s_cselect_b32 s62, s72, s71
	s_lshl_b32 s28, s62, 6
	v_or_b32_e32 v170, s28, v1
	v_lshl_add_u64 v[130:131], s[68:69], 0, v[170:171]
	v_lshlrev_b64 v[130:131], 7, v[130:131]
	v_lshl_add_u64 v[130:131], v[176:177], 0, v[130:131]
	v_mov_b32_e32 v215, v0
	s_barrier
	global_load_dword v170, v[130:131], off
	s_add_u32 s28, s68, s28
	v_mul_hi_i32 v130, v215, s54
	v_lshrrev_b32_e32 v131, 31, v130
	v_ashrrev_i32_e32 v130, 5, v130
	s_addc_u32 s29, s69, 0
	v_add_u32_e32 v242, v130, v131
	s_mulk_i32 s29, 0xc00
	s_mul_hi_u32 s30, s28, 0xc00
	v_mul_lo_u32 v130, v242, s55
	s_add_i32 s30, s30, s29
	s_mulk_i32 s28, 0xc00
	v_sub_u32_e32 v244, v215, v130
	s_add_u32 s28, s58, s28
	v_cmp_gt_i32_e32 vcc, 64, v244
	s_addc_u32 s29, s59, s30
	v_lshlrev_b32_e32 v243, 3, v244
	v_cndmask_b32_e32 v130, v212, v213, vcc
	v_add_u32_e32 v130, v130, v243
	v_mov_b64_e32 v[132:133], s[28:29]
	v_mad_i64_i32 v[134:135], s[28:29], v242, s53, v[132:133]
	v_ashrrev_i32_e32 v131, 31, v130
	v_lshl_add_u64 v[130:131], v[130:131], 1, v[134:135]
	v_add_u32_e32 v134, 0x200, v215
	v_mul_hi_i32 v135, v134, s54
	v_lshrrev_b32_e32 v136, 31, v135
	v_ashrrev_i32_e32 v135, 5, v135
	v_add_u32_e32 v239, v135, v136
	v_mul_lo_u32 v135, v239, s55
	v_sub_u32_e32 v241, v134, v135
	v_cmp_gt_i32_e32 vcc, 64, v241
	v_lshlrev_b32_e32 v240, 3, v241
	v_mad_i64_i32 v[136:137], s[28:29], v239, s53, v[132:133]
	v_cndmask_b32_e32 v134, v212, v213, vcc
	v_add_u32_e32 v134, v134, v240
	v_ashrrev_i32_e32 v135, 31, v134
	v_lshl_add_u64 v[134:135], v[134:135], 1, v[136:137]
	global_load_dwordx4 v[166:169], v[130:131], off nt
	global_load_dwordx4 v[162:165], v[134:135], off nt
	v_add_u32_e32 v130, 0x400, v215
	v_mul_hi_i32 v131, v130, s54
	v_lshrrev_b32_e32 v134, 31, v131
	v_ashrrev_i32_e32 v131, 5, v131
	v_add_u32_e32 v236, v131, v134
	v_mul_lo_u32 v131, v236, s55
	v_sub_u32_e32 v238, v130, v131
	v_cmp_gt_i32_e32 vcc, 64, v238
	v_lshlrev_b32_e32 v237, 3, v238
	v_mad_i64_i32 v[134:135], s[28:29], v236, s53, v[132:133]
	v_cndmask_b32_e32 v130, v212, v213, vcc
	v_add_u32_e32 v130, v130, v237
	v_ashrrev_i32_e32 v131, 31, v130
	v_lshl_add_u64 v[130:131], v[130:131], 1, v[134:135]
	v_add_u32_e32 v134, 0x600, v215
	v_mul_hi_i32 v135, v134, s54
	v_lshrrev_b32_e32 v136, 31, v135
	v_ashrrev_i32_e32 v135, 5, v135
	v_add_u32_e32 v233, v135, v136
	v_mul_lo_u32 v135, v233, s55
	v_sub_u32_e32 v235, v134, v135
	v_cmp_gt_i32_e32 vcc, 64, v235
	v_lshlrev_b32_e32 v234, 3, v235
	v_mad_i64_i32 v[136:137], s[28:29], v233, s53, v[132:133]
	v_cndmask_b32_e32 v134, v212, v213, vcc
	v_add_u32_e32 v134, v134, v234
	v_ashrrev_i32_e32 v135, 31, v134
	v_lshl_add_u64 v[134:135], v[134:135], 1, v[136:137]
	global_load_dwordx4 v[158:161], v[130:131], off nt
	global_load_dwordx4 v[154:157], v[134:135], off nt
	v_add_u32_e32 v130, 0x800, v215
	v_mul_hi_i32 v131, v130, s54
	v_lshrrev_b32_e32 v134, 31, v131
	v_ashrrev_i32_e32 v131, 5, v131
	v_add_u32_e32 v230, v131, v134
	v_mul_lo_u32 v131, v230, s55
	v_sub_u32_e32 v232, v130, v131
	v_cmp_gt_i32_e32 vcc, 64, v232
	v_lshlrev_b32_e32 v231, 3, v232
	v_mad_i64_i32 v[134:135], s[28:29], v230, s53, v[132:133]
	v_cndmask_b32_e32 v130, v212, v213, vcc
	v_add_u32_e32 v130, v130, v231
	v_ashrrev_i32_e32 v131, 31, v130
	v_lshl_add_u64 v[130:131], v[130:131], 1, v[134:135]
	v_add_u32_e32 v134, 0xa00, v215
	v_mul_hi_i32 v135, v134, s54
	v_lshrrev_b32_e32 v136, 31, v135
	v_ashrrev_i32_e32 v135, 5, v135
	v_add_u32_e32 v227, v135, v136
	v_mul_lo_u32 v135, v227, s55
	v_sub_u32_e32 v229, v134, v135
	v_cmp_gt_i32_e32 vcc, 64, v229
	v_lshlrev_b32_e32 v228, 3, v229
	v_mad_i64_i32 v[136:137], s[28:29], v227, s53, v[132:133]
	v_cndmask_b32_e32 v134, v212, v213, vcc
	v_add_u32_e32 v134, v134, v228
	v_ashrrev_i32_e32 v135, 31, v134
	v_lshl_add_u64 v[134:135], v[134:135], 1, v[136:137]
	global_load_dwordx4 v[150:153], v[130:131], off nt
	global_load_dwordx4 v[146:149], v[134:135], off nt
	v_add_u32_e32 v130, 0xc00, v215
	v_mul_hi_i32 v131, v130, s54
	v_lshrrev_b32_e32 v134, 31, v131
	v_ashrrev_i32_e32 v131, 5, v131
	v_add_u32_e32 v224, v131, v134
	v_mul_lo_u32 v131, v224, s55
	v_sub_u32_e32 v226, v130, v131
	v_cmp_gt_i32_e32 vcc, 64, v226
	v_lshlrev_b32_e32 v225, 3, v226
	v_mad_i64_i32 v[134:135], s[28:29], v224, s53, v[132:133]
	v_cndmask_b32_e32 v130, v212, v213, vcc
	v_add_u32_e32 v130, v130, v225
	v_ashrrev_i32_e32 v131, 31, v130
	v_lshl_add_u64 v[130:131], v[130:131], 1, v[134:135]
	v_add_u32_e32 v134, 0xe00, v215
	v_mul_hi_i32 v135, v134, s54
	v_lshrrev_b32_e32 v136, 31, v135
	v_ashrrev_i32_e32 v135, 5, v135
	v_add_u32_e32 v221, v135, v136
	v_mul_lo_u32 v135, v221, s55
	v_sub_u32_e32 v223, v134, v135
	v_cmp_gt_i32_e32 vcc, 64, v223
	v_lshlrev_b32_e32 v222, 3, v223
	v_mad_i64_i32 v[136:137], s[28:29], v221, s53, v[132:133]
	v_cndmask_b32_e32 v134, v212, v213, vcc
	v_add_u32_e32 v134, v134, v222
	v_ashrrev_i32_e32 v135, 31, v134
	v_lshl_add_u64 v[134:135], v[134:135], 1, v[136:137]
	global_load_dwordx4 v[142:145], v[130:131], off nt
	global_load_dwordx4 v[138:141], v[134:135], off nt
	v_add_u32_e32 v130, 0x1000, v215
	v_mul_hi_i32 v131, v130, s54
	v_lshrrev_b32_e32 v134, 31, v131
	v_ashrrev_i32_e32 v131, 5, v131
	v_add_u32_e32 v218, v131, v134
	v_mul_lo_u32 v131, v218, s55
	v_sub_u32_e32 v220, v130, v131
	v_cmp_gt_i32_e32 vcc, 64, v220
	v_lshlrev_b32_e32 v219, 3, v220
	v_mad_i64_i32 v[134:135], s[28:29], v218, s53, v[132:133]
	v_cndmask_b32_e32 v130, v212, v213, vcc
	v_add_u32_e32 v130, v130, v219
	v_ashrrev_i32_e32 v131, 31, v130
	v_lshl_add_u64 v[130:131], v[130:131], 1, v[134:135]
	v_add_u32_e32 v134, 0x1200, v215
	v_mul_hi_i32 v135, v134, s54
	v_lshrrev_b32_e32 v136, 31, v135
	v_ashrrev_i32_e32 v135, 5, v135
	v_add_u32_e32 v215, v135, v136
	v_mul_lo_u32 v135, v215, s55
	v_sub_u32_e32 v217, v134, v135
	v_cmp_gt_i32_e32 vcc, 64, v217
	v_lshlrev_b32_e32 v216, 3, v217
	v_mad_i64_i32 v[132:133], s[28:29], v215, s53, v[132:133]
	v_cndmask_b32_e32 v134, v212, v213, vcc
	v_add_u32_e32 v134, v134, v216
	v_ashrrev_i32_e32 v135, 31, v134
	v_lshl_add_u64 v[132:133], v[134:135], 1, v[132:133]
	global_load_dwordx4 v[134:137], v[130:131], off nt
	s_nop 0
	global_load_dwordx4 v[130:133], v[132:133], off nt
	v_and_b32_e32 v245, -16, v242
	v_lshlrev_b32_e32 v246, 1, v242
	v_cmp_lt_i32_e64 s[46:47], 63, v244
	v_cmp_lt_i32_e64 s[44:45], 63, v241
	v_cmp_lt_i32_e64 s[42:43], 63, v238
	v_cmp_lt_i32_e64 s[40:41], 63, v235
	v_cmp_lt_i32_e64 s[38:39], 63, v232
	v_cmp_lt_i32_e64 s[36:37], 63, v229
	v_cmp_lt_i32_e64 s[34:35], 63, v226
	v_cmp_lt_i32_e64 s[30:31], 63, v223
	v_cmp_lt_i32_e64 s[28:29], 63, v220
	v_cmp_lt_i32_e32 vcc, 63, v217
	v_and_or_b32 v247, v246, 8, v245
	s_and_saveexec_b64 s[74:75], s[46:47]
	s_xor_b64 s[46:47], exec, s[74:75]
	v_add_u32_e32 v245, 0xfffffe00, v243
	v_ashrrev_i32_e32 v243, 1, v247
	v_lshrrev_b32_e32 v244, 5, v245
	v_add_u32_e32 v246, v243, v244
	s_or_saveexec_b64 s[46:47], s[46:47]
	v_mov_b32_e32 v248, 0
	s_xor_b64 exec, exec, s[46:47]
	v_lshlrev_b32_e32 v244, 10, v244
	v_and_b32_e32 v244, 0xffffc000, v244
	v_add_u32_e32 v244, 0, v244
	v_and_b32_e32 v245, 0x78, v243
	v_add_u32_e32 v248, 0x8000, v244
	v_ashrrev_i32_e32 v244, 1, v247
	v_bfe_u32 v243, v243, 5, 2
	v_or_b32_e32 v246, v244, v243
	s_or_b64 exec, exec, s[46:47]
	v_lshrrev_b32_e32 v243, 1, v242
	v_and_b32_e32 v242, 3, v242
	v_and_or_b32 v242, v243, 4, v242
	v_lshlrev_b32_e32 v243, 1, v245
	v_lshlrev_b32_e32 v242, 6, v242
	v_and_b32_e32 v243, 48, v243
	v_lshl_add_u32 v244, v246, 9, v248
	v_add3_u32 v242, v244, v242, v243
	s_waitcnt vmcnt(9)
	ds_write_b128 v242, v[166:169]
	v_and_b32_e32 v166, -16, v239
	v_lshlrev_b32_e32 v167, 1, v239
	v_and_or_b32 v168, v167, 8, v166
	s_and_saveexec_b64 s[46:47], s[44:45]
	s_xor_b64 s[44:45], exec, s[46:47]
	v_add_u32_e32 v166, 0xfffffe00, v240
	v_ashrrev_i32_e32 v167, 1, v168
	v_lshrrev_b32_e32 v168, 5, v166
	v_add_u32_e32 v167, v167, v168
	s_or_saveexec_b64 s[44:45], s[44:45]
	v_mov_b32_e32 v169, 0
	s_xor_b64 exec, exec, s[44:45]
	v_lshlrev_b32_e32 v167, 10, v241
	v_and_b32_e32 v167, 0xffffc000, v167
	v_add_u32_e32 v167, 0, v167
	v_add_u32_e32 v169, 0x8000, v167
	v_ashrrev_i32_e32 v167, 1, v168
	v_bfe_u32 v168, v240, 5, 2
	v_and_b32_e32 v166, 0x78, v240
	v_or_b32_e32 v167, v167, v168
	s_or_b64 exec, exec, s[44:45]
	v_lshrrev_b32_e32 v168, 1, v239
	v_and_b32_e32 v239, 3, v239
	v_and_or_b32 v168, v168, 4, v239
	v_lshlrev_b32_e32 v166, 1, v166
	v_lshlrev_b32_e32 v168, 6, v168
	v_and_b32_e32 v166, 48, v166
	v_lshl_add_u32 v167, v167, 9, v169
	v_add3_u32 v166, v167, v168, v166
	s_waitcnt vmcnt(8)
	ds_write_b128 v166, v[162:165]
	v_and_b32_e32 v162, -16, v236
	v_lshlrev_b32_e32 v163, 1, v236
	v_and_or_b32 v164, v163, 8, v162
	s_and_saveexec_b64 s[44:45], s[42:43]
	s_xor_b64 s[42:43], exec, s[44:45]
	v_add_u32_e32 v162, 0xfffffe00, v237
	v_ashrrev_i32_e32 v163, 1, v164
	v_lshrrev_b32_e32 v164, 5, v162
	v_add_u32_e32 v163, v163, v164
	s_or_saveexec_b64 s[42:43], s[42:43]
	v_mov_b32_e32 v165, 0
	s_xor_b64 exec, exec, s[42:43]
	v_lshlrev_b32_e32 v163, 10, v238
	v_and_b32_e32 v163, 0xffffc000, v163
	v_add_u32_e32 v163, 0, v163
	v_add_u32_e32 v165, 0x8000, v163
	v_ashrrev_i32_e32 v163, 1, v164
	v_bfe_u32 v164, v237, 5, 2
	v_and_b32_e32 v162, 0x78, v237
	v_or_b32_e32 v163, v163, v164
	s_or_b64 exec, exec, s[42:43]
	v_lshrrev_b32_e32 v164, 1, v236
	v_and_b32_e32 v166, 3, v236
	v_and_or_b32 v164, v164, 4, v166
	v_lshlrev_b32_e32 v162, 1, v162
	v_lshlrev_b32_e32 v164, 6, v164
	v_and_b32_e32 v162, 48, v162
	v_lshl_add_u32 v163, v163, 9, v165
	v_add3_u32 v162, v163, v164, v162
	s_waitcnt vmcnt(7)
	ds_write_b128 v162, v[158:161]
	v_and_b32_e32 v158, -16, v233
	v_lshlrev_b32_e32 v159, 1, v233
	v_and_or_b32 v160, v159, 8, v158
	s_and_saveexec_b64 s[42:43], s[40:41]
	s_xor_b64 s[40:41], exec, s[42:43]
	v_add_u32_e32 v158, 0xfffffe00, v234
	v_ashrrev_i32_e32 v159, 1, v160
	v_lshrrev_b32_e32 v160, 5, v158
	v_add_u32_e32 v159, v159, v160
	s_or_saveexec_b64 s[40:41], s[40:41]
	v_mov_b32_e32 v161, 0
	s_xor_b64 exec, exec, s[40:41]
	v_lshlrev_b32_e32 v159, 10, v235
	v_and_b32_e32 v159, 0xffffc000, v159
	v_add_u32_e32 v159, 0, v159
	v_add_u32_e32 v161, 0x8000, v159
	v_ashrrev_i32_e32 v159, 1, v160
	v_bfe_u32 v160, v234, 5, 2
	v_and_b32_e32 v158, 0x78, v234
	v_or_b32_e32 v159, v159, v160
	s_or_b64 exec, exec, s[40:41]
	v_lshrrev_b32_e32 v160, 1, v233
	v_and_b32_e32 v162, 3, v233
	v_and_or_b32 v160, v160, 4, v162
	v_lshlrev_b32_e32 v158, 1, v158
	v_lshlrev_b32_e32 v160, 6, v160
	v_and_b32_e32 v158, 48, v158
	v_lshl_add_u32 v159, v159, 9, v161
	v_add3_u32 v158, v159, v160, v158
	s_waitcnt vmcnt(6)
	ds_write_b128 v158, v[154:157]
	v_and_b32_e32 v154, -16, v230
	v_lshlrev_b32_e32 v155, 1, v230
	v_and_or_b32 v156, v155, 8, v154
	s_and_saveexec_b64 s[40:41], s[38:39]
	s_xor_b64 s[38:39], exec, s[40:41]
	v_add_u32_e32 v154, 0xfffffe00, v231
	v_ashrrev_i32_e32 v155, 1, v156
	v_lshrrev_b32_e32 v156, 5, v154
	v_add_u32_e32 v155, v155, v156
	s_or_saveexec_b64 s[38:39], s[38:39]
	v_mov_b32_e32 v157, 0
	s_xor_b64 exec, exec, s[38:39]
	v_lshlrev_b32_e32 v155, 10, v232
	v_and_b32_e32 v155, 0xffffc000, v155
	v_add_u32_e32 v155, 0, v155
	v_add_u32_e32 v157, 0x8000, v155
	v_ashrrev_i32_e32 v155, 1, v156
	v_bfe_u32 v156, v231, 5, 2
	v_and_b32_e32 v154, 0x78, v231
	v_or_b32_e32 v155, v155, v156
	s_or_b64 exec, exec, s[38:39]
	v_lshrrev_b32_e32 v156, 1, v230
	v_and_b32_e32 v158, 3, v230
	v_and_or_b32 v156, v156, 4, v158
	v_lshlrev_b32_e32 v154, 1, v154
	v_lshlrev_b32_e32 v156, 6, v156
	v_and_b32_e32 v154, 48, v154
	v_lshl_add_u32 v155, v155, 9, v157
	v_add3_u32 v154, v155, v156, v154
	s_waitcnt vmcnt(5)
	ds_write_b128 v154, v[150:153]
	v_and_b32_e32 v150, -16, v227
	v_lshlrev_b32_e32 v151, 1, v227
	v_and_or_b32 v152, v151, 8, v150
	s_and_saveexec_b64 s[38:39], s[36:37]
	s_xor_b64 s[36:37], exec, s[38:39]
	v_add_u32_e32 v150, 0xfffffe00, v228
	v_ashrrev_i32_e32 v151, 1, v152
	v_lshrrev_b32_e32 v152, 5, v150
	v_add_u32_e32 v151, v151, v152
	s_or_saveexec_b64 s[36:37], s[36:37]
	v_mov_b32_e32 v153, 0
	s_xor_b64 exec, exec, s[36:37]
	v_lshlrev_b32_e32 v151, 10, v229
	v_and_b32_e32 v151, 0xffffc000, v151
	v_add_u32_e32 v151, 0, v151
	v_add_u32_e32 v153, 0x8000, v151
	v_ashrrev_i32_e32 v151, 1, v152
	v_bfe_u32 v152, v228, 5, 2
	v_and_b32_e32 v150, 0x78, v228
	v_or_b32_e32 v151, v151, v152
	s_or_b64 exec, exec, s[36:37]
	v_lshrrev_b32_e32 v152, 1, v227
	v_and_b32_e32 v154, 3, v227
	v_and_or_b32 v152, v152, 4, v154
	v_lshlrev_b32_e32 v150, 1, v150
	v_lshlrev_b32_e32 v152, 6, v152
	v_and_b32_e32 v150, 48, v150
	v_lshl_add_u32 v151, v151, 9, v153
	v_add3_u32 v150, v151, v152, v150
	s_waitcnt vmcnt(4)
	ds_write_b128 v150, v[146:149]
	v_and_b32_e32 v146, -16, v224
	v_lshlrev_b32_e32 v147, 1, v224
	v_and_or_b32 v148, v147, 8, v146
	s_and_saveexec_b64 s[36:37], s[34:35]
	s_xor_b64 s[34:35], exec, s[36:37]
	v_add_u32_e32 v146, 0xfffffe00, v225
	v_ashrrev_i32_e32 v147, 1, v148
	v_lshrrev_b32_e32 v148, 5, v146
	v_add_u32_e32 v147, v147, v148
	s_or_saveexec_b64 s[34:35], s[34:35]
	v_mov_b32_e32 v149, 0
	s_xor_b64 exec, exec, s[34:35]
	v_lshlrev_b32_e32 v147, 10, v226
	v_and_b32_e32 v147, 0xffffc000, v147
	v_add_u32_e32 v147, 0, v147
	v_add_u32_e32 v149, 0x8000, v147
	v_ashrrev_i32_e32 v147, 1, v148
	v_bfe_u32 v148, v225, 5, 2
	v_and_b32_e32 v146, 0x78, v225
	v_or_b32_e32 v147, v147, v148
	s_or_b64 exec, exec, s[34:35]
	v_lshrrev_b32_e32 v148, 1, v224
	v_and_b32_e32 v150, 3, v224
	v_and_or_b32 v148, v148, 4, v150
	v_lshlrev_b32_e32 v146, 1, v146
	v_lshlrev_b32_e32 v148, 6, v148
	v_and_b32_e32 v146, 48, v146
	v_lshl_add_u32 v147, v147, 9, v149
	v_add3_u32 v146, v147, v148, v146
	s_waitcnt vmcnt(3)
	ds_write_b128 v146, v[142:145]
	v_and_b32_e32 v142, -16, v221
	v_lshlrev_b32_e32 v143, 1, v221
	v_and_or_b32 v144, v143, 8, v142
	s_and_saveexec_b64 s[34:35], s[30:31]
	s_xor_b64 s[30:31], exec, s[34:35]
	v_add_u32_e32 v142, 0xfffffe00, v222
	v_ashrrev_i32_e32 v143, 1, v144
	v_lshrrev_b32_e32 v144, 5, v142
	v_add_u32_e32 v143, v143, v144
	s_or_saveexec_b64 s[30:31], s[30:31]
	v_mov_b32_e32 v145, 0
	s_xor_b64 exec, exec, s[30:31]
	v_lshlrev_b32_e32 v143, 10, v223
	v_and_b32_e32 v143, 0xffffc000, v143
	v_add_u32_e32 v143, 0, v143
	v_add_u32_e32 v145, 0x8000, v143
	v_ashrrev_i32_e32 v143, 1, v144
	v_bfe_u32 v144, v222, 5, 2
	v_and_b32_e32 v142, 0x78, v222
	v_or_b32_e32 v143, v143, v144
	s_or_b64 exec, exec, s[30:31]
	v_lshrrev_b32_e32 v144, 1, v221
	v_and_b32_e32 v146, 3, v221
	v_and_or_b32 v144, v144, 4, v146
	v_lshlrev_b32_e32 v142, 1, v142
	v_lshlrev_b32_e32 v144, 6, v144
	v_and_b32_e32 v142, 48, v142
	v_lshl_add_u32 v143, v143, 9, v145
	v_add3_u32 v142, v143, v144, v142
	s_waitcnt vmcnt(2)
	ds_write_b128 v142, v[138:141]
	v_and_b32_e32 v138, -16, v218
	v_lshlrev_b32_e32 v139, 1, v218
	v_and_or_b32 v140, v139, 8, v138
	s_and_saveexec_b64 s[30:31], s[28:29]
	s_xor_b64 s[28:29], exec, s[30:31]
	v_add_u32_e32 v138, 0xfffffe00, v219
	v_ashrrev_i32_e32 v139, 1, v140
	v_lshrrev_b32_e32 v140, 5, v138
	v_add_u32_e32 v139, v139, v140
	s_or_saveexec_b64 s[28:29], s[28:29]
	v_mov_b32_e32 v141, 0
	s_xor_b64 exec, exec, s[28:29]
	v_lshlrev_b32_e32 v139, 10, v220
	v_and_b32_e32 v139, 0xffffc000, v139
	v_add_u32_e32 v139, 0, v139
	v_add_u32_e32 v141, 0x8000, v139
	v_ashrrev_i32_e32 v139, 1, v140
	v_bfe_u32 v140, v219, 5, 2
	v_and_b32_e32 v138, 0x78, v219
	v_or_b32_e32 v139, v139, v140
	s_or_b64 exec, exec, s[28:29]
	v_lshrrev_b32_e32 v140, 1, v218
	v_and_b32_e32 v142, 3, v218
	v_and_or_b32 v140, v140, 4, v142
	v_lshlrev_b32_e32 v138, 1, v138
	v_lshlrev_b32_e32 v140, 6, v140
	v_and_b32_e32 v138, 48, v138
	v_lshl_add_u32 v139, v139, 9, v141
	v_add3_u32 v138, v139, v140, v138
	s_waitcnt vmcnt(1)
	ds_write_b128 v138, v[134:137]
	v_and_b32_e32 v134, -16, v215
	v_lshlrev_b32_e32 v135, 1, v215
	v_and_or_b32 v136, v135, 8, v134
	s_and_saveexec_b64 s[28:29], vcc
	s_xor_b64 s[28:29], exec, s[28:29]
	v_add_u32_e32 v134, 0xfffffe00, v216
	v_ashrrev_i32_e32 v135, 1, v136
	v_lshrrev_b32_e32 v136, 5, v134
	v_add_u32_e32 v135, v135, v136
	s_or_saveexec_b64 s[28:29], s[28:29]
	v_mov_b32_e32 v137, 0
	s_xor_b64 exec, exec, s[28:29]
	v_lshlrev_b32_e32 v135, 10, v217
	v_and_b32_e32 v135, 0xffffc000, v135
	v_add_u32_e32 v135, 0, v135
	v_add_u32_e32 v137, 0x8000, v135
	v_ashrrev_i32_e32 v135, 1, v136
	v_bfe_u32 v136, v216, 5, 2
	v_and_b32_e32 v134, 0x78, v216
	v_or_b32_e32 v135, v135, v136
	s_or_b64 exec, exec, s[28:29]
	v_lshrrev_b32_e32 v136, 1, v215
	v_and_b32_e32 v138, 3, v215
	v_and_or_b32 v136, v136, 4, v138
	v_lshlrev_b32_e32 v134, 1, v134
	v_lshlrev_b32_e32 v136, 6, v136
	v_and_b32_e32 v134, 48, v134
	v_lshl_add_u32 v135, v135, 9, v137
	v_add3_u32 v134, v135, v136, v134
	s_waitcnt vmcnt(0)
	ds_write_b128 v134, v[130:133]
	v_mul_f32_e64 v130, v170, -v191
	s_andn2_b64 vcc, exec, s[64:65]
	s_mov_b64 s[28:29], -1
	s_cbranch_vccnz .LBB0_404
	ds_bpermute_b32 v131, v180, v130
	s_mov_b64 s[28:29], 0
	s_waitcnt lgkmcnt(0)
	v_add_f32_e32 v131, v130, v131
	v_cndmask_b32_e64 v131, v131, v130, s[6:7]
	ds_bpermute_b32 v132, v181, v131
	s_waitcnt lgkmcnt(0)
	v_add_f32_e32 v132, v131, v132
	v_cndmask_b32_e64 v131, v131, v132, s[8:9]
	ds_bpermute_b32 v132, v182, v131
	s_waitcnt lgkmcnt(0)
	v_add_f32_e32 v132, v131, v132
	v_cndmask_b32_e64 v131, v131, v132, s[10:11]
	ds_bpermute_b32 v132, v183, v131
	s_waitcnt lgkmcnt(0)
	v_add_f32_e32 v132, v131, v132
	v_cndmask_b32_e64 v131, v131, v132, s[12:13]
	ds_bpermute_b32 v132, v184, v131
	s_waitcnt lgkmcnt(0)
	v_add_f32_e32 v132, v131, v132
	v_cndmask_b32_e64 v131, v131, v132, s[14:15]
	ds_bpermute_b32 v132, v178, v131
	s_waitcnt lgkmcnt(0)
	v_add_f32_e32 v132, v131, v132
	v_cndmask_b32_e64 v131, v131, v132, s[16:17]
